# speedup vs baseline: 1.0078x; 1.0078x over previous
.LBB3_11:
	v_and_b32_e32 v133, 64, v222
	v_xor_b32_e32 v132, 16, v222
	v_add_u32_e32 v133, 64, v133
	v_cmp_lt_i32_e64 s[2:3], v132, v133
	v_exp_f32_e32 v134, v114
	v_exp_f32_e32 v136, v116
	v_cndmask_b32_e64 v132, v222, v132, s[2:3]
	v_lshlrev_b32_e32 v140, 2, v132
	v_xor_b32_e32 v132, 32, v222
	v_exp_f32_e32 v137, v117
	v_exp_f32_e32 v135, v115
	v_cmp_lt_i32_e64 s[2:3], v132, v133
	v_or_b32_e32 v130, s42, v209
	v_or_b32_e32 v131, s41, v210
	v_cndmask_b32_e64 v132, v222, v132, s[2:3]
	s_lshr_b32 s2, s41, 7
	v_add_u32_e32 v194, s2, v206
	v_lshlrev_b32_e32 v141, 7, v130
	v_lshlrev_b32_e32 v139, 2, v132
	v_lshlrev_b64 v[132:133], 14, v[194:195]
	v_and_b32_e32 v194, 0x7b700, v141
	v_add_u32_e32 v142, 0x400, v131
	v_pk_add_f32 v[136:137], v[136:137], 1.0 op_sel_hi:[1,0]
	v_pk_add_f32 v[144:145], v[134:135], 1.0 op_sel_hi:[1,0]
	v_lshl_add_u64 v[146:147], v[200:201], 0, v[194:195]
	v_lshrrev_b32_e32 v194, 6, v142
	v_rcp_f32_e64 v143, -v137
	v_rcp_f32_e64 v142, -v136
	v_rcp_f32_e64 v149, -v145
	v_rcp_f32_e64 v148, -v144
	v_exp_f32_e32 v154, v80
	v_pk_fma_f32 v[152:153], v[142:143], 2.0, 1.0 op_sel_hi:[1,0,0]
	v_exp_f32_e32 v155, v81
	v_pk_fma_f32 v[142:143], v[148:149], 2.0, 1.0 op_sel_hi:[1,0,0]
	v_exp_f32_e32 v148, v78
	v_exp_f32_e32 v149, v79
	v_pk_add_f32 v[154:155], v[154:155], 1.0 op_sel_hi:[1,0]
	v_cvt_pk_bf16_f32 v142, v142, v143
	v_rcp_f32_e64 v157, -v155
	v_pk_add_f32 v[148:149], v[148:149], 1.0 op_sel_hi:[1,0]
	v_rcp_f32_e64 v156, -v154
	v_rcp_f32_e64 v159, -v149
	v_rcp_f32_e64 v158, -v148
	v_cvt_pk_bf16_f32 v143, v152, v153
	v_pk_fma_f32 v[152:153], v[156:157], 2.0, 1.0 op_sel_hi:[1,0,0]
	v_pk_mul_f32 v[148:149], v[144:145], v[148:149]
	v_pk_fma_f32 v[156:157], v[158:159], 2.0, 1.0 op_sel_hi:[1,0,0]
	v_cvt_pk_bf16_f32 v145, v152, v153
	v_cvt_pk_bf16_f32 v144, v156, v157
	v_exp_f32_e32 v152, v106
	v_exp_f32_e32 v153, v107
	v_exp_f32_e32 v156, v108
	v_exp_f32_e32 v157, v109
	v_pk_mul_f32 v[136:137], v[136:137], v[154:155]
	v_pk_add_f32 v[152:153], v[152:153], 1.0 op_sel_hi:[1,0]
	v_pk_add_f32 v[116:117], v[116:117], 0 op_sel_hi:[1,0]
	v_pk_add_f32 v[156:157], v[156:157], 1.0 op_sel_hi:[1,0]
	v_rcp_f32_e64 v163, -v153
	v_rcp_f32_e64 v161, -v157
	v_rcp_f32_e64 v160, -v156
	v_rcp_f32_e64 v162, -v152
	v_pk_mul_f32 v[148:149], v[148:149], v[152:153]
	v_pk_mul_f32 v[136:137], v[136:137], v[156:157]
	v_exp_f32_e32 v152, v70
	v_exp_f32_e32 v156, v72
	v_exp_f32_e32 v157, v73
	v_exp_f32_e32 v153, v71
	v_pk_add_f32 v[114:115], v[114:115], 0 op_sel_hi:[1,0]
	v_pk_add_f32 v[154:155], v[116:117], v[80:81]
	v_pk_add_f32 v[158:159], v[114:115], v[78:79]
	v_pk_add_f32 v[108:109], v[154:155], v[108:109]
	v_pk_add_f32 v[154:155], v[156:157], 1.0 op_sel_hi:[1,0]
	v_pk_add_f32 v[152:153], v[152:153], 1.0 op_sel_hi:[1,0]
	v_lshlrev_b64 v[134:135], 19, v[194:195]
	v_pk_add_f32 v[106:107], v[158:159], v[106:107]
	v_rcp_f32_e64 v157, -v155
	v_rcp_f32_e64 v156, -v154
	v_rcp_f32_e64 v159, -v153
	v_rcp_f32_e64 v158, -v152
	v_lshl_add_u64 v[150:151], v[146:147], 0, v[134:135]
	v_lshlrev_b32_e32 v194, 1, v198
	v_add_u32_e32 v138, s43, v207
	v_permlane16_swap_b32_e32 v142, v144
	v_permlane16_swap_b32_e32 v143, v145
	v_lshl_add_u64 v[150:151], v[150:151], 0, v[194:195]
	ds_read_b128 v[114:117], v138
	ds_read_b128 v[78:81], v138 offset:64
	global_store_dwordx4 v[150:151], v[142:145], off
	s_bitcmp1_b32 s20, 12
	s_cbranch_scc1 .Lg1_noX
	s_barrier
.Lg1_noX:
	v_pk_fma_f32 v[156:157], v[156:157], 2.0, 1.0 op_sel_hi:[1,0,0]
	v_pk_mul_f32 v[154:155], v[136:137], v[154:155]
	v_pk_fma_f32 v[144:145], v[160:161], 2.0, 1.0 op_sel_hi:[1,0,0]
	v_pk_fma_f32 v[142:143], v[162:163], 2.0, 1.0 op_sel_hi:[1,0,0]
	v_pk_mul_f32 v[148:149], v[148:149], v[152:153]
	v_cvt_pk_bf16_f32 v142, v142, v143
	v_cvt_pk_bf16_f32 v143, v144, v145
	v_pk_fma_f32 v[144:145], v[158:159], 2.0, 1.0 op_sel_hi:[1,0,0]
	v_pk_add_f32 v[152:153], v[108:109], v[72:73]
	v_cvt_pk_bf16_f32 v144, v144, v145
	v_cvt_pk_bf16_f32 v145, v156, v157
	s_nop 0
	v_permlane16_swap_b32_e32 v142, v144
	v_permlane16_swap_b32_e32 v143, v145
	v_pk_add_f32 v[158:159], v[106:107], v[70:71]
	ds_read_b128 v[106:109], v138 offset:128
	ds_read_b128 v[70:73], v138 offset:192
	global_store_dwordx4 v[150:151], v[142:145], off offset:128
	v_exp_f32_e32 v136, v90
	v_exp_f32_e32 v137, v91
	v_exp_f32_e32 v142, v92
	v_exp_f32_e32 v143, v93
	v_add_u32_e32 v131, 0x480, v131
	v_pk_add_f32 v[150:151], v[136:137], 1.0 op_sel_hi:[1,0]
	v_ashrrev_i32_e32 v144, 6, v131
	v_pk_add_f32 v[142:143], v[142:143], 1.0 op_sel_hi:[1,0]
	v_rcp_f32_e64 v161, -v151
	v_rcp_f32_e64 v157, -v143
	v_rcp_f32_e64 v156, -v142
	v_rcp_f32_e64 v160, -v150
	v_pk_mul_f32 v[148:149], v[148:149], v[150:151]
	v_pk_mul_f32 v[150:151], v[154:155], v[142:143]
	v_exp_f32_e32 v142, v42
	v_exp_f32_e32 v154, v44
	v_exp_f32_e32 v155, v45
	v_exp_f32_e32 v143, v43
	v_ashrrev_i32_e32 v145, 31, v144
	v_pk_add_f32 v[92:93], v[152:153], v[92:93]
	v_pk_add_f32 v[152:153], v[154:155], 1.0 op_sel_hi:[1,0]
	v_pk_add_f32 v[154:155], v[142:143], 1.0 op_sel_hi:[1,0]
	v_lshlrev_b64 v[136:137], 19, v[144:145]
	v_pk_fma_f32 v[144:145], v[156:157], 2.0, 1.0 op_sel_hi:[1,0,0]
	v_pk_fma_f32 v[156:157], v[160:161], 2.0, 1.0 op_sel_hi:[1,0,0]
	v_pk_add_f32 v[90:91], v[158:159], v[90:91]
	v_rcp_f32_e64 v159, -v153
	v_rcp_f32_e64 v158, -v152
	v_rcp_f32_e64 v161, -v155
	v_rcp_f32_e64 v160, -v154
	v_cvt_pk_bf16_f32 v142, v156, v157
	v_cvt_pk_bf16_f32 v143, v144, v145
	v_pk_fma_f32 v[156:157], v[158:159], 2.0, 1.0 op_sel_hi:[1,0,0]
	v_pk_fma_f32 v[144:145], v[160:161], 2.0, 1.0 op_sel_hi:[1,0,0]
	v_exp_f32_e32 v158, v128
	v_cvt_pk_bf16_f32 v144, v144, v145
	v_cvt_pk_bf16_f32 v145, v156, v157
	v_exp_f32_e32 v156, v126
	v_exp_f32_e32 v159, v129
	v_exp_f32_e32 v157, v127
	v_lshl_add_u64 v[146:147], v[146:147], 0, v[136:137]
	v_pk_mul_f32 v[150:151], v[150:151], v[152:153]
	v_pk_mul_f32 v[148:149], v[148:149], v[154:155]
	v_pk_add_f32 v[158:159], v[158:159], 1.0 op_sel_hi:[1,0]
	v_pk_add_f32 v[156:157], v[156:157], 1.0 op_sel_hi:[1,0]
	v_lshl_add_u64 v[164:165], v[146:147], 0, v[194:195]
	v_rcp_f32_e64 v163, -v157
	v_rcp_f32_e64 v162, -v156
	v_pk_mul_f32 v[146:147], v[148:149], v[156:157]
	v_pk_mul_f32 v[148:149], v[150:151], v[158:159]
	v_exp_f32_e32 v150, v58
	v_exp_f32_e32 v156, v60
	v_exp_f32_e32 v157, v61
	v_exp_f32_e32 v151, v59
	v_pk_add_f32 v[152:153], v[92:93], v[44:45]
	v_pk_add_f32 v[154:155], v[90:91], v[42:43]
	v_pk_add_f32 v[128:129], v[152:153], v[128:129]
	v_pk_add_f32 v[152:153], v[156:157], 1.0 op_sel_hi:[1,0]
	v_pk_add_f32 v[150:151], v[150:151], 1.0 op_sel_hi:[1,0]
	v_pk_mul_f32 v[148:149], v[148:149], v[152:153]
	v_pk_mul_f32 v[146:147], v[146:147], v[150:151]
	v_pk_add_f32 v[126:127], v[154:155], v[126:127]
	v_log_f32_e32 v131, v146
	v_log_f32_e32 v146, v147
	v_log_f32_e32 v147, v148
	v_log_f32_e32 v148, v149
	v_pk_add_f32 v[60:61], v[128:129], v[60:61]
	v_pk_add_f32 v[58:59], v[126:127], v[58:59]
	v_add_f32_e32 v126, v131, v146
	v_add_f32_e32 v127, v147, v148
	v_add_f32_e32 v58, v58, v59
	v_add_f32_e32 v59, v60, v61
	v_add_f32_e32 v126, v126, v127
	v_add_f32_e32 v58, v58, v59
	v_add_f32_e32 v126, 0xc2000000, v126
	v_mul_f32_e32 v131, 0xbeb17218, v58
	v_fmac_f32_e32 v131, 0x3f317218, v126
	v_rcp_f32_e64 v161, -v159
	v_rcp_f32_e64 v160, -v158
	ds_bpermute_b32 v148, v140, v131
	v_rcp_f32_e64 v155, -v153
	v_rcp_f32_e64 v154, -v152
	v_permlane16_swap_b32_e32 v142, v144
	v_permlane16_swap_b32_e32 v143, v145
	ds_read_b128 v[90:93], v138 offset:512
	ds_read_b128 v[42:45], v138 offset:576
	global_store_dwordx4 v[164:165], v[142:145], off
	v_rcp_f32_e64 v157, -v151
	v_rcp_f32_e64 v156, -v150
	v_pk_fma_f32 v[142:143], v[160:161], 2.0, 1.0 op_sel_hi:[1,0,0]
	v_pk_fma_f32 v[144:145], v[162:163], 2.0, 1.0 op_sel_hi:[1,0,0]
	s_waitcnt lgkmcnt(0)
	v_add_f32_e32 v131, v131, v148
	v_cvt_pk_bf16_f32 v144, v144, v145
	v_cvt_pk_bf16_f32 v145, v142, v143
	v_pk_fma_f32 v[142:143], v[154:155], 2.0, 1.0 op_sel_hi:[1,0,0]
	ds_read_b128 v[126:129], v138 offset:640
	ds_read_b128 v[58:61], v138 offset:704
	v_cvt_pk_bf16_f32 v147, v142, v143
	ds_bpermute_b32 v142, v139, v131
	v_pk_fma_f32 v[154:155], v[156:157], 2.0, 1.0 op_sel_hi:[1,0,0]
	v_lshl_add_u64 v[132:133], s[14:15], 0, v[132:133]
	v_cvt_pk_bf16_f32 v146, v154, v155
	s_nop 1
	v_permlane16_swap_b32_e32 v144, v146
	v_permlane16_swap_b32_e32 v145, v147
	global_store_dwordx4 v[164:165], v[144:147], off offset:128
	s_and_saveexec_b64 s[2:3], s[0:1]
	s_cbranch_execz .LBB3_13
	s_waitcnt lgkmcnt(0)
	v_add_f32_e32 v144, v131, v142
	v_mov_b32_e32 v131, v195
	v_lshl_add_u64 v[142:143], v[130:131], 2, v[132:133]
	global_store_dword v[142:143], v144, off

.LBB3_17:
	s_or_b64 exec, exec, s[2:3]
	s_bitcmp1_b32 s20, 12
	s_cbranch_scc0 .Lg1_noY
	s_barrier
.Lg1_noY:
	s_waitcnt lgkmcnt(0)
	v_exp_f32_e32 v142, v18
	v_exp_f32_e32 v144, v20
	v_exp_f32_e32 v145, v21
	v_exp_f32_e32 v143, v19
	v_exp_f32_e32 v154, v4
	v_exp_f32_e32 v155, v5
	v_pk_add_f32 v[144:145], v[144:145], 1.0 op_sel_hi:[1,0]
	v_pk_add_f32 v[148:149], v[142:143], 1.0 op_sel_hi:[1,0]
	v_rcp_f32_e64 v143, -v145
	v_rcp_f32_e64 v142, -v144
	v_rcp_f32_e64 v151, -v149
	v_rcp_f32_e64 v150, -v148
	v_pk_add_f32 v[154:155], v[154:155], 1.0 op_sel_hi:[1,0]
	v_pk_fma_f32 v[152:153], v[142:143], 2.0, 1.0 op_sel_hi:[1,0,0]
	v_rcp_f32_e64 v157, -v155
	v_pk_fma_f32 v[142:143], v[150:151], 2.0, 1.0 op_sel_hi:[1,0,0]
	v_exp_f32_e32 v150, v2
	v_exp_f32_e32 v151, v3
	v_rcp_f32_e64 v156, -v154
	v_cvt_pk_bf16_f32 v142, v142, v143
	v_cvt_pk_bf16_f32 v143, v152, v153
	v_pk_add_f32 v[150:151], v[150:151], 1.0 op_sel_hi:[1,0]
	v_pk_fma_f32 v[152:153], v[156:157], 2.0, 1.0 op_sel_hi:[1,0,0]
	v_rcp_f32_e64 v159, -v151
	v_rcp_f32_e64 v158, -v150
	v_pk_mul_f32 v[154:155], v[144:145], v[154:155]
	v_cvt_pk_bf16_f32 v145, v152, v153
	v_exp_f32_e32 v152, v26
	v_pk_fma_f32 v[156:157], v[158:159], 2.0, 1.0 op_sel_hi:[1,0,0]
	v_exp_f32_e32 v153, v27
	v_cvt_pk_bf16_f32 v144, v156, v157
	v_exp_f32_e32 v156, v28
	v_exp_f32_e32 v157, v29
	v_pk_mul_f32 v[148:149], v[148:149], v[150:151]
	v_pk_add_f32 v[152:153], v[152:153], 1.0 op_sel_hi:[1,0]
	v_pk_add_f32 v[20:21], v[20:21], 0 op_sel_hi:[1,0]
	v_pk_add_f32 v[156:157], v[156:157], 1.0 op_sel_hi:[1,0]
	v_rcp_f32_e64 v163, -v153
	v_rcp_f32_e64 v161, -v157
	v_rcp_f32_e64 v160, -v156
	v_rcp_f32_e64 v162, -v152
	v_pk_mul_f32 v[148:149], v[148:149], v[152:153]
	v_pk_mul_f32 v[152:153], v[154:155], v[156:157]
	v_exp_f32_e32 v154, v10
	v_exp_f32_e32 v156, v12
	v_exp_f32_e32 v157, v13
	v_exp_f32_e32 v155, v11
	v_pk_add_f32 v[18:19], v[18:19], 0 op_sel_hi:[1,0]
	v_pk_add_f32 v[150:151], v[20:21], v[4:5]
	v_bitop3_b32 v146, v141, s38, v225 bitop3:0xc8
	v_mov_b32_e32 v147, v195
	v_pk_add_f32 v[158:159], v[18:19], v[2:3]
	v_pk_add_f32 v[28:29], v[150:151], v[28:29]
	v_pk_add_f32 v[150:151], v[156:157], 1.0 op_sel_hi:[1,0]
	v_pk_add_f32 v[154:155], v[154:155], 1.0 op_sel_hi:[1,0]
	v_lshl_add_u64 v[146:147], v[200:201], 0, v[146:147]
	v_pk_add_f32 v[26:27], v[158:159], v[26:27]
	v_rcp_f32_e64 v157, -v151
	v_rcp_f32_e64 v156, -v150
	v_rcp_f32_e64 v159, -v155
	v_rcp_f32_e64 v158, -v154
	v_lshl_add_u64 v[134:135], v[146:147], 0, v[134:135]
	v_permlane16_swap_b32_e32 v142, v144
	v_permlane16_swap_b32_e32 v143, v145
	v_lshl_add_u64 v[134:135], v[134:135], 0, v[194:195]
	ds_read_b128 v[18:21], v138
	ds_read_b128 v[2:5], v138 offset:64
	global_store_dwordx4 v[134:135], v[142:145], off
	v_pk_fma_f32 v[156:157], v[156:157], 2.0, 1.0 op_sel_hi:[1,0,0]
	v_pk_mul_f32 v[150:151], v[152:153], v[150:151]
	v_pk_fma_f32 v[144:145], v[160:161], 2.0, 1.0 op_sel_hi:[1,0,0]
	v_pk_fma_f32 v[142:143], v[162:163], 2.0, 1.0 op_sel_hi:[1,0,0]
	v_pk_mul_f32 v[148:149], v[148:149], v[154:155]
	v_cvt_pk_bf16_f32 v142, v142, v143
	v_cvt_pk_bf16_f32 v143, v144, v145
	v_pk_fma_f32 v[144:145], v[158:159], 2.0, 1.0 op_sel_hi:[1,0,0]
	v_exp_f32_e32 v158, v24
	v_cvt_pk_bf16_f32 v144, v144, v145
	v_cvt_pk_bf16_f32 v145, v156, v157
	v_exp_f32_e32 v156, v22
	v_exp_f32_e32 v159, v25
	v_exp_f32_e32 v157, v23
	v_permlane16_swap_b32_e32 v142, v144
	v_permlane16_swap_b32_e32 v143, v145
	v_pk_add_f32 v[158:159], v[158:159], 1.0 op_sel_hi:[1,0]
	v_pk_add_f32 v[156:157], v[156:157], 1.0 op_sel_hi:[1,0]
	v_pk_add_f32 v[152:153], v[28:29], v[12:13]
	v_pk_add_f32 v[154:155], v[26:27], v[10:11]
	ds_read_b128 v[26:29], v138 offset:128
	ds_read_b128 v[10:13], v138 offset:192
	global_store_dwordx4 v[134:135], v[142:145], off offset:128
	v_rcp_f32_e64 v161, -v159
	v_rcp_f32_e64 v160, -v158
	v_lshl_add_u64 v[142:143], v[146:147], 0, v[136:137]
	v_pk_mul_f32 v[144:145], v[148:149], v[156:157]
	v_pk_mul_f32 v[146:147], v[150:151], v[158:159]
	v_exp_f32_e32 v148, v6
	v_exp_f32_e32 v150, v8
	v_exp_f32_e32 v151, v9
	v_exp_f32_e32 v149, v7
	v_rcp_f32_e64 v163, -v157
	v_rcp_f32_e64 v162, -v156
	v_pk_add_f32 v[150:151], v[150:151], 1.0 op_sel_hi:[1,0]
	v_pk_add_f32 v[148:149], v[148:149], 1.0 op_sel_hi:[1,0]
	v_pk_add_f32 v[24:25], v[152:153], v[24:25]
	v_pk_add_f32 v[22:23], v[154:155], v[22:23]
	v_rcp_f32_e64 v153, -v151
	v_rcp_f32_e64 v152, -v150
	v_rcp_f32_e64 v155, -v149
	v_rcp_f32_e64 v154, -v148
	v_pk_fma_f32 v[136:137], v[160:161], 2.0, 1.0 op_sel_hi:[1,0,0]
	v_pk_fma_f32 v[134:135], v[162:163], 2.0, 1.0 op_sel_hi:[1,0,0]
	v_pk_fma_f32 v[152:153], v[152:153], 2.0, 1.0 op_sel_hi:[1,0,0]
	v_cvt_pk_bf16_f32 v134, v134, v135
	v_cvt_pk_bf16_f32 v135, v136, v137
	v_pk_fma_f32 v[136:137], v[154:155], 2.0, 1.0 op_sel_hi:[1,0,0]
	v_pk_mul_f32 v[144:145], v[144:145], v[148:149]
	v_cvt_pk_bf16_f32 v136, v136, v137
	v_cvt_pk_bf16_f32 v137, v152, v153
	v_exp_f32_e32 v152, v30
	v_exp_f32_e32 v153, v31
	v_exp_f32_e32 v154, v32
	v_exp_f32_e32 v155, v33
	v_lshl_add_u64 v[160:161], v[142:143], 0, v[194:195]
	v_pk_add_f32 v[152:153], v[152:153], 1.0 op_sel_hi:[1,0]
	v_exp_f32_e32 v142, v14
	v_rcp_f32_e64 v159, -v153
	v_rcp_f32_e64 v158, -v152
	v_pk_mul_f32 v[144:145], v[144:145], v[152:153]
	v_exp_f32_e32 v152, v16
	v_exp_f32_e32 v153, v17
	v_exp_f32_e32 v143, v15
	v_pk_mul_f32 v[146:147], v[146:147], v[150:151]
	v_pk_add_f32 v[148:149], v[24:25], v[8:9]
	v_pk_add_f32 v[150:151], v[22:23], v[6:7]
	v_pk_add_f32 v[154:155], v[154:155], 1.0 op_sel_hi:[1,0]
	v_pk_add_f32 v[32:33], v[148:149], v[32:33]
	v_pk_mul_f32 v[146:147], v[146:147], v[154:155]
	v_pk_add_f32 v[30:31], v[150:151], v[30:31]
	v_pk_add_f32 v[148:149], v[152:153], 1.0 op_sel_hi:[1,0]
	v_pk_add_f32 v[150:151], v[142:143], 1.0 op_sel_hi:[1,0]
	v_pk_mul_f32 v[146:147], v[146:147], v[148:149]
	v_pk_mul_f32 v[144:145], v[144:145], v[150:151]
	v_pk_add_f32 v[16:17], v[32:33], v[16:17]
	v_log_f32_e32 v131, v144
	v_log_f32_e32 v141, v145
	v_log_f32_e32 v144, v146
	v_log_f32_e32 v145, v147
	v_pk_add_f32 v[14:15], v[30:31], v[14:15]
	v_add_f32_e32 v30, v131, v141
	v_add_f32_e32 v14, v14, v15
	v_add_f32_e32 v31, v144, v145
	v_add_f32_e32 v15, v16, v17
	v_add_f32_e32 v30, v30, v31
	v_add_f32_e32 v14, v14, v15
	v_add_f32_e32 v30, 0xc2000000, v30
	v_mul_f32_e32 v131, 0xbeb17218, v14
	v_fmac_f32_e32 v131, 0x3f317218, v30
	v_rcp_f32_e64 v157, -v155
	v_rcp_f32_e64 v156, -v154
	ds_bpermute_b32 v140, v140, v131
	v_rcp_f32_e64 v153, -v149
	v_rcp_f32_e64 v152, -v148
	v_permlane16_swap_b32_e32 v134, v136
	v_permlane16_swap_b32_e32 v135, v137
	ds_read_b128 v[22:25], v138 offset:512
	ds_read_b128 v[6:9], v138 offset:576
	global_store_dwordx4 v[160:161], v[134:137], off
	v_rcp_f32_e64 v155, -v151
	v_rcp_f32_e64 v154, -v150
	v_pk_fma_f32 v[134:135], v[156:157], 2.0, 1.0 op_sel_hi:[1,0,0]
	s_waitcnt lgkmcnt(0)
	v_add_f32_e32 v131, v131, v140
	v_cvt_pk_bf16_f32 v143, v134, v135
	v_pk_fma_f32 v[134:135], v[152:153], 2.0, 1.0 op_sel_hi:[1,0,0]
	ds_read_b128 v[30:33], v138 offset:640
	ds_read_b128 v[14:17], v138 offset:704
	v_cvt_pk_bf16_f32 v145, v134, v135
	ds_bpermute_b32 v134, v139, v131
	v_pk_fma_f32 v[136:137], v[158:159], 2.0, 1.0 op_sel_hi:[1,0,0]
	v_permlane16_swap_b32_e32 v143, v145
	v_cvt_pk_bf16_f32 v142, v136, v137
	v_pk_fma_f32 v[136:137], v[154:155], 2.0, 1.0 op_sel_hi:[1,0,0]
	s_nop 0
	v_cvt_pk_bf16_f32 v144, v136, v137
	s_nop 1
	v_permlane16_swap_b32_e32 v142, v144
	global_store_dwordx4 v[160:161], v[142:145], off offset:128
	s_and_saveexec_b64 s[2:3], s[0:1]
	s_cbranch_execz .LBB3_5
	s_waitcnt lgkmcnt(0)
	v_add_f32_e32 v134, v131, v134
	v_mov_b32_e32 v131, v195
	v_lshl_add_u64 v[130:131], v[130:131], 2, v[132:133]
	global_store_dword v[130:131], v134, off offset:576
	s_branch .LBB3_5
